# P6 epilogue: x pointer loaded once with s_load, residual loads no longer wait behind a pointer round trip
# speedup vs baseline: 1.0053x; 1.0020x over previous
; #define IN(k) (fresh_tid(C), lo <= (k) && (k) < hi)
; #define SEAM(k) do { if (IN(k) && IN((k) + 1)) xcd_barrier(bar); } while (0)
;     __host__ __device__ bool map(int i, int& pm, int& pn) const {
;         const int L = i * G + c; if (L >= nwg || c < 0) return false;
;         int wgid = L; { const int q = nwg / NXCD, r = nwg % NXCD, xcd = wgid % NXCD, off = wgid / NXCD; wgid = (xcd < r ? xcd * (q + 1) : r * (q + 1) + (xcd - r) * q) + off; }
;         const int nig = WGM * nN, gid = wgid / nig, fm = gid * WGM, gsz = (nM - fm) < WGM ? (nM - fm) : WGM;
;         pm = fm + ((wgid % nig) % gsz); pn = (wgid % nig) / gsz; return true;
; __global__ void __launch_bounds__(512, 2) mk_fwd(Args args) {
;     ...
;     if (IN(6)) for (int rep_ = ((MK_REPEAT >> 6) & 1) ? 0 : 1; rep_ < 2; ++rep_) { pg8::Gemm g{WSP(bf16_t, WS_MIX), WSP(bf16_t, WS_WOUT), T_, D_, MIXP / 2}; pg8::StaticOrder S; S.init(T_, D_, C.G, C.bid); pg8::EpiResF32 E{C.ka, C.ws, D_, rep_ ? WS_ROWSS : WS_PROJ, 1.0f / (MIX_SCALE * W_FP8_SCALE)};
;         pg8::gemm_phase<pg8::EpiResF32, pg8::StaticOrder, false, 2>(C.lds, g, S, E); if (!rep_) xcd_barrier(bar); } SEAM(6);
.LBB0_803:
	s_cmp_lt_i32 s82, 7
	s_cselect_b64 s[0:1], -1, 0
	s_cmp_gt_i32 s83, 6
	v_mov_b32_e32 v1, v0
	s_cselect_b64 s[2:3], -1, 0
	s_and_b64 s[0:1], s[0:1], s[2:3]
	v_cndmask_b32_e64 v1, 0, 1, s[0:1]
	v_cmp_ne_u32_e64 s[4:5], 1, v1
	s_andn2_b64 vcc, exec, s[0:1]
	s_mov_b64 s[54:55], s[80:81]
	s_cbranch_vccnz .LBB0_840
	s_load_dwordx2 s[96:97], s[54:55], 0x0
	s_waitcnt lgkmcnt(0)
	v_readlane_b32 s0, v254, 0
	v_readlane_b32 s1, v254, 1
	s_mov_b32 s2, s0
	s_cmpk_lt_u32 s0, 0x400
	v_mov_b32_e32 v2, v0
	s_cselect_b64 s[0:1], -1, 0
	s_cmpk_gt_u32 s2, 0x3ff
	s_nop 0
	v_readfirstlane_b32 s17, v2
	s_cbranch_scc1 .LBB0_806
	v_readlane_b32 s2, v254, 0
	v_readlane_b32 s3, v254, 1
	s_mov_b32 s6, s2
	s_lshl_b32 s2, s2, 7
	s_lshr_b32 s3, s6, 3
	s_or_b32 s2, s2, s3
	s_lshr_b32 s2, s2, 3
	s_and_b32 s2, s2, 0x78
	s_bfe_u32 s3, s6, 0x30003
	s_or_b32 s46, s2, s3
	s_bfe_u32 s45, s6, 0x30006

.LBB0_820:
	ds_read_b128 v[130:133], v159
	ds_read_b128 v[134:137], v159 offset:1024
	ds_read_b128 v[138:141], v159 offset:2048
	ds_read_b128 v[142:145], v159 offset:3072
	s_add_i32 s14, s20, 0xfffb0080
	s_cmp_eq_u32 s49, 16
	s_cselect_b32 s52, s1, s14
	s_cselect_b32 s50, s0, s21
	s_or_b32 s51, s52, 0x80
	s_mov_b32 m0, s38
	ds_read_b128 v[146:149], v160
	ds_read_b128 v[150:153], v160 offset:1024
	ds_read_b128 v[166:169], v160 offset:2048
	ds_read_b128 v[170:173], v160 offset:3072
	ds_read_b128 v[174:177], v160 offset:4096
	ds_read_b128 v[178:181], v160 offset:5120
	ds_read_b128 v[182:185], v160 offset:6144
	ds_read_b128 v[186:189], v160 offset:7168
	buffer_load_dwordx4 v155, s[8:11], s20 offen lds
	s_mov_b32 m0, s39
	s_nop 0
	buffer_load_dwordx4 v156, s[8:11], s20 offen lds
	s_waitcnt lgkmcnt(8)
	s_barrier
	s_waitcnt lgkmcnt(0)
	s_setprio 1
	s_waitcnt lgkmcnt(6)
	v_mfma_f32_16x16x128_f8f6f4 v[126:129], v[130:137], v[146:153], v[126:129]
	v_mfma_f32_16x16x128_f8f6f4 v[122:125], v[138:145], v[146:153], v[122:125]
	s_waitcnt lgkmcnt(4)
	v_mfma_f32_16x16x128_f8f6f4 v[190:193], v[130:137], v[166:173], v[110:113]
	v_mfma_f32_16x16x128_f8f6f4 v[194:197], v[138:145], v[166:173], v[106:109]
	s_waitcnt lgkmcnt(2)
	v_mfma_f32_16x16x128_f8f6f4 v[198:201], v[130:137], v[174:181], v[94:97]
	v_mfma_f32_16x16x128_f8f6f4 v[202:205], v[138:145], v[174:181], v[90:93]
	s_waitcnt lgkmcnt(0)
	v_mfma_f32_16x16x128_f8f6f4 v[206:209], v[130:137], v[182:189], v[78:81]
	v_mfma_f32_16x16x128_f8f6f4 v[210:213], v[138:145], v[182:189], v[74:77]
	s_setprio 0
	s_barrier
	s_mov_b32 s14, s10
	s_mov_b32 s15, s11
	s_mov_b32 m0, s23
	s_nop 1
	ds_read_b128 v[74:77], v161
	ds_read_b128 v[78:81], v161 offset:1024
	ds_read_b128 v[90:93], v161 offset:2048
	ds_read_b128 v[94:97], v161 offset:3072
	buffer_load_dwordx4 v1, s[12:15], s50 offen lds
	s_mov_b32 m0, s24
	s_nop 0
	buffer_load_dwordx4 v154, s[12:15], s50 offen lds
	s_barrier
	s_waitcnt lgkmcnt(0)
	s_setprio 1
	s_waitcnt lgkmcnt(2)
	v_mfma_f32_16x16x128_f8f6f4 v[118:121], v[74:81], v[146:153], v[118:121]
	s_waitcnt lgkmcnt(0)
	v_mfma_f32_16x16x128_f8f6f4 v[114:117], v[90:97], v[146:153], v[114:117]
	v_mfma_f32_16x16x128_f8f6f4 v[146:149], v[74:81], v[166:173], v[102:105]
	v_mfma_f32_16x16x128_f8f6f4 v[150:153], v[90:97], v[166:173], v[98:101]
	v_mfma_f32_16x16x128_f8f6f4 v[166:169], v[74:81], v[174:181], v[86:89]
	v_mfma_f32_16x16x128_f8f6f4 v[170:173], v[90:97], v[174:181], v[82:85]
	v_mfma_f32_16x16x128_f8f6f4 v[174:177], v[74:81], v[182:189], v[70:73]
	v_mfma_f32_16x16x128_f8f6f4 v[178:181], v[90:97], v[182:189], v[66:69]
	s_setprio 0
	s_mov_b32 m0, s22
	s_barrier
	s_nop 3
	ds_read_b128 v[66:69], v160 offset:16384
	ds_read_b128 v[70:73], v160 offset:17408
	ds_read_b128 v[82:85], v160 offset:18432
	ds_read_b128 v[86:89], v160 offset:19456
	ds_read_b128 v[98:101], v160 offset:20480
	ds_read_b128 v[102:105], v160 offset:21504
	ds_read_b128 v[106:109], v160 offset:22528
	ds_read_b128 v[110:113], v160 offset:23552
	buffer_load_dwordx4 v155, s[8:11], s52 offen lds
	s_mov_b32 m0, s25
	s_nop 0
	buffer_load_dwordx4 v156, s[8:11], s52 offen lds
	s_barrier
	s_waitcnt lgkmcnt(0)
	s_setprio 1
	s_waitcnt lgkmcnt(6)
	v_mfma_f32_16x16x128_f8f6f4 v[62:65], v[130:137], v[66:73], v[62:65]
	v_mfma_f32_16x16x128_f8f6f4 v[58:61], v[138:145], v[66:73], v[58:61]
	s_waitcnt lgkmcnt(4)
	v_mfma_f32_16x16x128_f8f6f4 v[182:185], v[130:137], v[82:89], v[46:49]
	v_mfma_f32_16x16x128_f8f6f4 v[186:189], v[138:145], v[82:89], v[42:45]
	s_waitcnt lgkmcnt(2)
	v_mfma_f32_16x16x128_f8f6f4 v[214:217], v[130:137], v[98:105], v[22:25]
	v_mfma_f32_16x16x128_f8f6f4 v[218:221], v[138:145], v[98:105], v[18:21]
	s_waitcnt lgkmcnt(0)
	v_mfma_f32_16x16x128_f8f6f4 v[222:225], v[130:137], v[106:113], v[6:9]
	v_mfma_f32_16x16x128_f8f6f4 v[226:229], v[138:145], v[106:113], v[2:5]
	s_setprio 0
	s_barrier
	s_add_i32 s53, s50, 0x50000
	s_mov_b32 m0, s26
	s_nop 0
	buffer_load_dwordx4 v1, s[12:15], s53 offen lds
	s_mov_b32 m0, s27
	s_nop 0
	buffer_load_dwordx4 v154, s[12:15], s53 offen lds
	s_waitcnt vmcnt(6)
	s_barrier
	s_setprio 1
	v_mfma_f32_16x16x128_f8f6f4 v[54:57], v[74:81], v[66:73], v[54:57]
	v_mfma_f32_16x16x128_f8f6f4 v[50:53], v[90:97], v[66:73], v[50:53]
	v_mfma_f32_16x16x128_f8f6f4 v[230:233], v[74:81], v[82:89], v[38:41]
	v_mfma_f32_16x16x128_f8f6f4 v[234:237], v[90:97], v[82:89], v[34:37]
	v_mfma_f32_16x16x128_f8f6f4 v[238:241], v[74:81], v[98:105], v[30:33]
	v_mfma_f32_16x16x128_f8f6f4 v[242:245], v[90:97], v[98:105], v[26:29]
	v_mfma_f32_16x16x128_f8f6f4 v[246:249], v[74:81], v[106:113], v[14:17]
	v_mfma_f32_16x16x128_f8f6f4 v[250:253], v[90:97], v[106:113], v[10:13]
	s_setprio 0
	s_barrier
	ds_read_b128 v[2:5], v162
	ds_read_b128 v[6:9], v162 offset:1024
	s_nop 2
	ds_read_b128 v[10:13], v162 offset:2048
	ds_read_b128 v[14:17], v162 offset:3072
	s_add_i32 s52, s52, 0x50000
	s_mov_b32 m0, s28
	ds_read_b128 v[18:21], v160 offset:32768
	ds_read_b128 v[22:25], v160 offset:33792
	ds_read_b128 v[26:29], v160 offset:34816
	ds_read_b128 v[30:33], v160 offset:35840
	ds_read_b128 v[34:37], v160 offset:36864
	ds_read_b128 v[38:41], v160 offset:37888
	ds_read_b128 v[42:45], v160 offset:38912
	ds_read_b128 v[46:49], v160 offset:39936
	buffer_load_dwordx4 v155, s[8:11], s52 offen lds
	s_mov_b32 m0, s29
	s_nop 0
	buffer_load_dwordx4 v156, s[8:11], s52 offen lds
	s_waitcnt lgkmcnt(8)
	s_barrier
	s_waitcnt lgkmcnt(0)
	s_setprio 1
	s_waitcnt lgkmcnt(6)
	v_mfma_f32_16x16x128_f8f6f4 v[126:129], v[2:9], v[18:25], v[126:129]
	v_mfma_f32_16x16x128_f8f6f4 v[122:125], v[10:17], v[18:25], v[122:125]
	s_waitcnt lgkmcnt(4)
	v_mfma_f32_16x16x128_f8f6f4 v[110:113], v[2:9], v[26:33], v[190:193]
	v_mfma_f32_16x16x128_f8f6f4 v[106:109], v[10:17], v[26:33], v[194:197]
	s_waitcnt lgkmcnt(2)
	v_mfma_f32_16x16x128_f8f6f4 v[94:97], v[2:9], v[34:41], v[198:201]
	v_mfma_f32_16x16x128_f8f6f4 v[90:93], v[10:17], v[34:41], v[202:205]
	s_waitcnt lgkmcnt(0)
	v_mfma_f32_16x16x128_f8f6f4 v[78:81], v[2:9], v[42:49], v[206:209]
	v_mfma_f32_16x16x128_f8f6f4 v[74:77], v[10:17], v[42:49], v[210:213]
	s_setprio 0
	s_barrier
	s_or_b32 s52, s50, 0x80
	s_mov_b32 m0, s31
	ds_read_b128 v[130:133], v163
	ds_read_b128 v[134:137], v163 offset:1024
	ds_read_b128 v[138:141], v163 offset:2048
	ds_read_b128 v[142:145], v163 offset:3072
	buffer_load_dwordx4 v1, s[12:15], s52 offen lds
	s_mov_b32 m0, s33
	s_nop 0
	buffer_load_dwordx4 v154, s[12:15], s52 offen lds
	s_barrier
	s_waitcnt lgkmcnt(0)
	s_setprio 1
	s_waitcnt lgkmcnt(2)
	v_mfma_f32_16x16x128_f8f6f4 v[118:121], v[130:137], v[18:25], v[118:121]
	s_waitcnt lgkmcnt(0)
	v_mfma_f32_16x16x128_f8f6f4 v[114:117], v[138:145], v[18:25], v[114:117]
	v_mfma_f32_16x16x128_f8f6f4 v[102:105], v[130:137], v[26:33], v[146:149]
	v_mfma_f32_16x16x128_f8f6f4 v[98:101], v[138:145], v[26:33], v[150:153]
	v_mfma_f32_16x16x128_f8f6f4 v[86:89], v[130:137], v[34:41], v[166:169]
	v_mfma_f32_16x16x128_f8f6f4 v[82:85], v[138:145], v[34:41], v[170:173]
	v_mfma_f32_16x16x128_f8f6f4 v[70:73], v[130:137], v[42:49], v[174:177]
	v_mfma_f32_16x16x128_f8f6f4 v[66:69], v[138:145], v[42:49], v[178:181]
	s_setprio 0
	s_mov_b32 m0, s34
	s_barrier
	ds_read_b128 v[26:29], v160 offset:49152
	ds_read_b128 v[30:33], v160 offset:50176
	ds_read_b128 v[146:149], v160 offset:51200
	ds_read_b128 v[150:153], v160 offset:52224
	ds_read_b128 v[166:169], v160 offset:53248
	ds_read_b128 v[170:173], v160 offset:54272
	ds_read_b128 v[174:177], v160 offset:55296
	ds_read_b128 v[178:181], v160 offset:56320
	buffer_load_dwordx4 v155, s[8:11], s51 offen lds
	s_mov_b32 m0, s35
	s_nop 0
	buffer_load_dwordx4 v156, s[8:11], s51 offen lds
	s_barrier
	s_waitcnt lgkmcnt(0)
	s_setprio 1
	s_waitcnt lgkmcnt(6)
	v_mfma_f32_16x16x128_f8f6f4 v[62:65], v[2:9], v[26:33], v[62:65]
	v_mfma_f32_16x16x128_f8f6f4 v[58:61], v[10:17], v[26:33], v[58:61]
	s_waitcnt lgkmcnt(4)
	v_mfma_f32_16x16x128_f8f6f4 v[46:49], v[2:9], v[146:153], v[182:185]
	v_mfma_f32_16x16x128_f8f6f4 v[42:45], v[10:17], v[146:153], v[186:189]
	s_waitcnt lgkmcnt(2)
	v_mfma_f32_16x16x128_f8f6f4 v[22:25], v[2:9], v[166:173], v[214:217]
	v_mfma_f32_16x16x128_f8f6f4 v[18:21], v[10:17], v[166:173], v[218:221]
	s_waitcnt lgkmcnt(0)
	v_mfma_f32_16x16x128_f8f6f4 v[6:9], v[2:9], v[174:181], v[222:225]
	v_mfma_f32_16x16x128_f8f6f4 v[2:5], v[10:17], v[174:181], v[226:229]
	s_setprio 0
	s_barrier
	s_add_i32 s50, s50, 0x50080
	s_mov_b32 m0, s36
	s_nop 0
	buffer_load_dwordx4 v1, s[12:15], s50 offen lds
	s_mov_b32 m0, s37
	s_nop 0
	buffer_load_dwordx4 v154, s[12:15], s50 offen lds
	s_waitcnt vmcnt(6)
	s_barrier
	s_setprio 1
	v_mfma_f32_16x16x128_f8f6f4 v[54:57], v[130:137], v[26:33], v[54:57]
	v_mfma_f32_16x16x128_f8f6f4 v[50:53], v[138:145], v[26:33], v[50:53]
	v_mfma_f32_16x16x128_f8f6f4 v[38:41], v[130:137], v[146:153], v[230:233]
	v_mfma_f32_16x16x128_f8f6f4 v[34:37], v[138:145], v[146:153], v[234:237]
	v_mfma_f32_16x16x128_f8f6f4 v[30:33], v[130:137], v[166:173], v[238:241]
	v_mfma_f32_16x16x128_f8f6f4 v[26:29], v[138:145], v[166:173], v[242:245]
	v_mfma_f32_16x16x128_f8f6f4 v[14:17], v[130:137], v[174:181], v[246:249]
	v_mfma_f32_16x16x128_f8f6f4 v[10:13], v[138:145], v[174:181], v[250:253]
	s_setprio 0
	s_add_i32 s49, s49, 2
	s_addk_i32 s20, 0x100
	s_addk_i32 s21, 0x100
	s_cmp_gt_u32 s49, 17
	s_barrier
	s_cbranch_scc0 .LBB0_820
; #define LAS __attribute__((address_space(3)))
;     __device__ __forceinline__ void operator()(const f32x4 (&acc)[2][2][4][2], const Unit& u, int wr, int wc, int fr, int fq, LAS const unsigned char* tbl, LAS const unsigned char* b2l) const {
;         const int row0 = u.pm * BM + wr * 64 + fr, col0 = u.pn * BM + wc * 32 + 8 * fq;
;         const float* __restrict__ rp = args_in(ka, 0); _Float16* __restrict__ cp = (_Float16*)(ws + WS_X1H); float* rowss = (float*)(ws + rowss_off);
; #pragma unroll
;         for (int ai = 0; ai < 2; ++ai)
; #pragma unroll
;             for (int mp = 0; mp < 2; ++mp) { f32x4 r[2][2][2];
; #pragma unroll
;                 for (int mm = 0; mm < 2; ++mm) { const size_t off = (size_t)(row0 + ai * HALF + (2 * mp + mm) * 16) * ldc + col0;
; #pragma unroll
;                     for (int bj = 0; bj < 2; ++bj)
; #pragma unroll
;                         for (int n = 0; n < 2; ++n) r[mm][bj][n] = __builtin_nontemporal_load((const f32x4*)(rp + off + bj * HALF + n * 4)); }
; #pragma unroll
;                 for (int mm = 0; mm < 2; ++mm) { const int m = 2 * mp + mm; const int row = row0 + ai * HALF + m * 16; const size_t off = (size_t)row * ldc + col0; float ss = 0.f;
; #pragma unroll
;                     for (int bj = 0; bj < 2; ++bj) { const f32x4 o0 = r[mm][bj][0] + acc[ai][bj][m][0] * scale, o1 = r[mm][bj][1] + acc[ai][bj][m][1] * scale;
;                         ss += ((o0[0] * o0[0] + o0[1] * o0[1]) + (o0[2] * o0[2] + o0[3] * o0[3])) + ((o1[0] * o1[0] + o1[1] * o1[1]) + (o1[2] * o1[2] + o1[3] * o1[3]));
;                         f16x8 h;
; #pragma unroll
;                         for (int j = 0; j < 4; ++j) { h[j] = (_Float16)__builtin_amdgcn_fmed3f(o0[j], -65504.0f, 65504.0f); h[4 + j] = (_Float16)__builtin_amdgcn_fmed3f(o1[j], -65504.0f, 65504.0f); }
;                         *(f16x8*)(cp + off + bj * HALF) = h; }
;                     ss += __shfl_xor(ss, 16); ss += __shfl_xor(ss, 32);
;                     if (fq == 0) rowss[(size_t)row * 32 + u.pn * 4 + wc] = ss; } }
	v_mov_b64_e32 v[130:131], s[96:97]
	s_nop 0
	v_lshl_add_u32 v148, s46, 8, v157
	v_lshl_or_b32 v146, s45, 8, v158
	v_ashrrev_i32_e32 v147, 31, v146
	v_ashrrev_i32_e32 v149, 31, v148
	v_lshlrev_b64 v[132:133], 13, v[148:149]
	v_or_b32_e32 v152, 16, v148
	v_ashrrev_i32_e32 v153, 31, v152
	v_and_b32_e32 v167, 64, v164
	v_xor_b32_e32 v166, 16, v164
	v_add_u32_e32 v167, 64, v167
	v_xor_b32_e32 v184, 32, v164
	v_cmp_lt_i32_e32 vcc, v166, v167
	s_lshl_b32 s0, s45, 2
	s_ashr_i32 s1, s0, 31
	v_cndmask_b32_e32 v166, v164, v166, vcc
	v_cmp_lt_i32_e32 vcc, v184, v167
	v_lshlrev_b32_e32 v167, 2, v166
	s_lshl_b64 s[0:1], s[0:1], 2
	v_cndmask_b32_e32 v186, v164, v184, vcc
	v_lshlrev_b64 v[184:185], 12, v[148:149]
	v_lshlrev_b32_e32 v166, 2, v186
	s_add_u32 s14, s40, s0
	s_addc_u32 s15, s41, s1
	s_waitcnt lgkmcnt(0)
	v_lshl_add_u64 v[150:151], v[146:147], 2, v[130:131]
	v_lshl_add_u64 v[130:131], v[150:151], 0, v[132:133]
	global_load_dwordx4 v[168:171], v[130:131], off nt
	global_load_dwordx4 v[172:175], v[130:131], off offset:16 nt
	global_load_dwordx4 v[176:179], v[130:131], off offset:512 nt
	global_load_dwordx4 v[180:183], v[130:131], off offset:528 nt
	v_lshlrev_b64 v[130:131], 13, v[152:153]
	v_lshl_add_u64 v[130:131], v[150:151], 0, v[130:131]
	global_load_dwordx4 v[142:145], v[130:131], off nt
	global_load_dwordx4 v[138:141], v[130:131], off offset:16 nt
	global_load_dwordx4 v[134:137], v[130:131], off offset:512 nt
	s_nop 0
	global_load_dwordx4 v[130:133], v[130:131], off offset:528 nt
	v_lshl_add_u64 v[146:147], v[146:147], 1, s[2:3]
	v_lshl_add_u64 v[184:185], v[146:147], 0, v[184:185]
	s_waitcnt vmcnt(0) lgkmcnt(0)
	v_add_u32_e32 v188, 0x20, v148
	v_ashrrev_i32_e32 v189, 31, v188
	v_lshlrev_b64 v[188:189], 13, v[188:189]
	v_lshl_add_u64 v[188:189], v[150:151], 0, v[188:189]
	global_load_dwordx4 v[190:193], v[188:189], off nt
	global_load_dwordx4 v[194:197], v[188:189], off offset:16 nt
	global_load_dwordx4 v[198:201], v[188:189], off offset:512 nt
	global_load_dwordx4 v[202:205], v[188:189], off offset:528 nt
	v_add_u32_e32 v188, 0x30, v148
	v_ashrrev_i32_e32 v189, 31, v188
	v_lshlrev_b64 v[188:189], 13, v[188:189]
	v_lshl_add_u64 v[188:189], v[150:151], 0, v[188:189]
	global_load_dwordx4 v[206:209], v[188:189], off nt
	global_load_dwordx4 v[210:213], v[188:189], off offset:16 nt
	global_load_dwordx4 v[214:217], v[188:189], off offset:512 nt
	global_load_dwordx4 v[218:221], v[188:189], off offset:528 nt
	v_pk_fma_f32 v[128:129], v[128:129], s[16:17], v[170:171] op_sel_hi:[1,0,1]
	v_pk_fma_f32 v[126:127], v[126:127], s[16:17], v[168:169] op_sel_hi:[1,0,1]
	v_pk_fma_f32 v[124:125], v[124:125], s[16:17], v[174:175] op_sel_hi:[1,0,1]
	v_pk_fma_f32 v[122:123], v[122:123], s[16:17], v[172:173] op_sel_hi:[1,0,1]
	v_pk_fma_f32 v[120:121], v[120:121], s[16:17], v[178:179] op_sel_hi:[1,0,1]
	v_pk_fma_f32 v[118:119], v[118:119], s[16:17], v[176:177] op_sel_hi:[1,0,1]
	v_pk_fma_f32 v[168:169], v[116:117], s[16:17], v[182:183] op_sel_hi:[1,0,1]
	v_pk_fma_f32 v[170:171], v[114:115], s[16:17], v[180:181] op_sel_hi:[1,0,1]
	v_mul_f32_e32 v172, v127, v127
	v_mul_f32_e32 v173, v129, v129
	v_mul_f32_e32 v174, v123, v123
	v_mul_f32_e32 v175, v125, v125
	v_med3_f32 v114, v126, s42, v165
	v_med3_f32 v116, v122, s42, v165
	v_med3_f32 v127, v127, s42, v165
	v_med3_f32 v123, v123, s42, v165
	v_med3_f32 v115, v128, s42, v165
	v_med3_f32 v117, v124, s42, v165
	v_med3_f32 v129, v129, s42, v165
	v_med3_f32 v125, v125, s42, v165
	v_mul_f32_e32 v176, v119, v119
	v_mul_f32_e32 v177, v121, v121
	v_mul_f32_e32 v178, v171, v171
	v_mul_f32_e32 v179, v169, v169
	v_fmac_f32_e32 v172, v126, v126
	v_fmac_f32_e32 v173, v128, v128
	v_fmac_f32_e32 v174, v122, v122
	v_fmac_f32_e32 v175, v124, v124
	v_cvt_pk_f16_f32 v117, v117, v125
	v_cvt_pk_f16_f32 v115, v115, v129
	v_cvt_pk_f16_f32 v116, v116, v123
	v_cvt_pk_f16_f32 v114, v114, v127
	v_fmac_f32_e32 v176, v118, v118
	v_fmac_f32_e32 v177, v120, v120
	v_fmac_f32_e32 v178, v170, v170
	v_fmac_f32_e32 v179, v168, v168
	v_med3_f32 v180, v118, s42, v165
	v_med3_f32 v182, v119, s42, v165
	v_add_f32_e32 v118, v172, v173
	v_add_f32_e32 v119, v174, v175
	global_store_dwordx4 v[184:185], v[114:117], off
	v_med3_f32 v181, v170, s42, v165
	v_med3_f32 v171, v171, s42, v165
	v_add_f32_e32 v114, v176, v177
	v_add_f32_e32 v115, v178, v179
	v_add_f32_e32 v116, v118, v119
	v_add_f32_e32 v114, v114, v115
	v_add_f32_e32 v114, v116, v114
	ds_bpermute_b32 v115, v167, v114
	v_med3_f32 v117, v120, s42, v165
	v_med3_f32 v116, v168, s42, v165
	v_med3_f32 v118, v121, s42, v165
	v_med3_f32 v119, v169, s42, v165
	s_waitcnt lgkmcnt(0)
	v_add_f32_e32 v114, v114, v115
	ds_bpermute_b32 v115, v166, v114
	v_cvt_pk_f16_f32 v119, v116, v119
	v_cvt_pk_f16_f32 v117, v117, v118
	v_cvt_pk_f16_f32 v118, v181, v171
	v_cvt_pk_f16_f32 v116, v180, v182
	global_store_dwordx4 v[184:185], v[116:119], off offset:256
	s_and_saveexec_b64 s[0:1], s[6:7]
	s_cbranch_execz .LBB0_823
	v_lshlrev_b64 v[116:117], 7, v[148:149]
	v_lshl_add_u64 v[116:117], s[14:15], 0, v[116:117]
	s_waitcnt lgkmcnt(0)
	v_add_f32_e32 v114, v114, v115
	global_store_dword v[116:117], v114, off
